# PEER V loop second half: expert-row prefetch issued behind the token-start loads with a counted vmcnt(16) (token-end drain removed); final-norm gain slice parked per lane in LDS instead of four global
# baseline (speedup 1.0000x reference)
; #define V_RANGE(T, P, RLO, RHI, BLO, BHI) PL_RANGE4(T, P, RLO, RHI, BLO, BHI)
; #define V_RANGE(T, P, RLO, RHI, BLO, BHI) PL_RANGE(T, P, 2, RLO, RHI, BLO, BHI)
; __device__ __forceinline__ void peer_token_end(Frame& F, const Args& a, int layer, bool last, bool final_half, size_t tok, int lane, const f32x2 (&out)[8], const f32x4 (&hpre)[4], const v4u (&gpre)[2], const v4u& p8pre) {
;     ...
;     const float* g = (last ? a.in[4] : a.in[2] + (size_t)(layer + 1) * 1024) + 16 * lane;
; __device__ __forceinline__ void peer_unit(Frame& F, const Args& a, int layer, int unit, bool last) {
;     ...
;     for (int ps = DBG_V0; ps < VPASS; ++ps) {
;         int lt = 0, lb, lbh; { V_RANGE(lt, ps, r0, r1, b0_, b1_); lb = b0_; lbh = b1_; (void)r0; (void)r1; }
;         unsigned seL = sIdx[lane];
;         f32x2 out[8]; f32x4 hpre[4] = {(f32x4){0.f, 0.f, 0.f, 0.f}, (f32x4){0.f, 0.f, 0.f, 0.f}, (f32x4){0.f, 0.f, 0.f, 0.f}, (f32x4){0.f, 0.f, 0.f, 0.f}}, ac4[4]; v4u gpre[2] = {(v4u){0u, 0u, 0u, 0u}, (v4u){0u, 0u, 0u, 0u}}, p8pre = (v4u){0u, 0u, 0u, 0u}; const bf16* PWG = (const bf16*)(F.ws + WS_PW);
;         const unsigned vmask = ((lane >> 4) == ((lane & 15) >> 2)) ? (0xFFu << (8 * (lane & 3))) : 0u;
;         int ct, cb, crl = 0, crh = 0, cbl = 0, cbh = 0;
.LBB0_1779:
	v_lshrrev_b32_e32 v68, 2, v150
	v_and_b32_e32 v69, 24, v151
	s_movk_i32 s3, 0xff
	v_lshlrev_b32_e64 v69, v69, s3
	v_cmp_eq_u32_e32 vcc, v1, v68
	s_mov_b64 s[6:7], 0x1e00000
	v_lshl_add_u64 v[226:227], v[2:3], 0, s[6:7]
	v_cndmask_b32_e32 v249, 0, v69, vcc
	v_lshlrev_b64 v[2:3], 2, v[224:225]
	v_lshl_add_u64 v[68:69], v[224:225], 1, s[18:19]
	s_mov_b64 s[6:7], 0xe400000
	v_lshl_add_u64 v[228:229], s[20:21], 0, v[2:3]
	global_load_dwordx4 v[192:195], v[228:229], off offset:48
	global_load_dwordx4 v[196:199], v[228:229], off offset:32
	global_load_dwordx4 v[200:203], v[228:229], off offset:16
	global_load_dwordx4 v[204:207], v[228:229], off
	v_mov_b32_e32 v246, 0x1e000
	v_lshl_add_u32 v246, v224, 2, v246
	s_waitcnt vmcnt(0)
	ds_write_b128 v246, v[192:195] offset:48
	ds_write_b128 v246, v[196:199] offset:32
	ds_write_b128 v246, v[200:203] offset:16
	ds_write_b128 v246, v[204:207]
	v_lshl_add_u64 v[230:231], v[68:69], 0, s[6:7]
	v_lshl_add_u64 v[232:233], s[24:25], 0, v[2:3]
	v_lshl_add_u64 v[2:3], s[18:19], 0, v[224:225]
	s_mov_b64 s[6:7], 0x28400000
	s_mov_b32 s3, 0
	v_lshl_add_u64 v[234:235], v[2:3], 0, s[6:7]
	s_branch .LBB0_1781

; __device__ __forceinline__ void unpk8(const u32x4 w, f32x4& a, f32x4& b) { a = (f32x4){bflo(w.x), bfhi(w.x), bflo(w.y), bfhi(w.y)}; b = (f32x4){bflo(w.z), bfhi(w.z), bflo(w.w), bfhi(w.w)}; }
; __device__ __forceinline__ u32x4 pk8(const f32x4 a, const f32x4 b) { u32x4 w; w.x = cvt_pk_bf16(a[0], a[1]); w.y = cvt_pk_bf16(a[2], a[3]); w.z = cvt_pk_bf16(b[0], b[1]); w.w = cvt_pk_bf16(b[2], b[3]); return w; }
; __device__ __forceinline__ void peer_token_end(Frame& F, const Args& a, int layer, bool last, bool final_half, size_t tok, int lane, const f32x2 (&out)[8], const f32x4 (&hpre)[4], const v4u (&gpre)[2], const v4u& p8pre) {
;     ...
;     unpk8(gpre[0], ge[0], ge[1]); unpk8(gpre[1], ge[2], ge[3]);
; #pragma unroll
;     for (int i = 0; i < 4; ++i) { hv[i] = hpre[i] + ge[i] + pe[i];
;         s += (hv[i].x * hv[i].x + hv[i].y * hv[i].y) + (hv[i].z * hv[i].z + hv[i].w * hv[i].w); }
;     const float rstd = 1.f / sqrtf(wave_sum(s) * (1.f / D) + 1e-6f);
;     const float* g = (last ? a.in[4] : a.in[2] + (size_t)(layer + 1) * 1024) + 16 * lane;
;     f32x4 o[4];
; #pragma unroll
;     for (int i = 0; i < 4; ++i) o[i] = hv[i] * rstd * *(const f32x4*)(g + 4 * i);
;     if (last) {
;     ...
;         { const float pv = ((const float*)(F.ws + WS_CTL))[2048 + PROBE_SCAN - 1];
; #pragma unroll
;           for (int i = 0; i < 4; ++i) o[i] = o[i] + pv; }
;     ...
; #pragma unroll
;         for (int i = 0; i < 4; ++i) *(f32x4*)(hp + 4 * i) = o[i];
;     } else {
; #pragma unroll
;         for (int i = 0; i < 4; ++i) *(f32x4*)(hp + 4 * i) = hv[i];
;         bf16* NX = (bf16*)(F.ws + WS_NX) + NXROW(tok) * 1024 + 16 * lane; const v4u w0 = pk8(o[0], o[1]), w1 = pk8(o[2], o[3]);
;         *(v4u*)NX = w0; *(v4u*)(NX + 8) = w1;
.LBB0_1811:
	s_andn2_b64 vcc, exec, s[54:55]
	s_cbranch_vccnz .LBB0_1816
	v_lshlrev_b32_e32 v170, 16, v176
	v_and_b32_e32 v171, 0xffff0000, v176
	v_lshlrev_b32_e32 v194, 16, v177
	v_and_b32_e32 v195, 0xffff0000, v177
	v_pk_add_f32 v[236:237], v[128:129], v[170:171]
	v_pk_add_f32 v[170:171], v[130:131], v[194:195]
	v_lshlrev_b32_e32 v196, 16, v178
	v_pk_add_f32 v[170:171], v[170:171], v[168:169]
	v_pk_add_f32 v[168:169], v[236:237], v[174:175]
	v_mul_f32_e32 v174, v171, v171
	v_mul_f32_e32 v1, v169, v169
	v_and_b32_e32 v197, 0xffff0000, v178
	v_lshlrev_b32_e32 v198, 16, v179
	v_and_b32_e32 v199, 0xffff0000, v179
	v_fmac_f32_e32 v1, v168, v168
	v_fmac_f32_e32 v174, v170, v170
	v_add_f32_e32 v1, v1, v174
	v_pk_add_f32 v[194:195], v[132:133], v[196:197]
	v_pk_add_f32 v[174:175], v[134:135], v[198:199]
	v_lshlrev_b32_e32 v200, 16, v180
	v_pk_add_f32 v[174:175], v[174:175], v[172:173]
	v_pk_add_f32 v[172:173], v[194:195], v[184:185]
	v_mul_f32_e32 v185, v175, v175
	v_mul_f32_e32 v184, v173, v173
	v_fmac_f32_e32 v184, v172, v172
	v_fmac_f32_e32 v185, v174, v174
	v_and_b32_e32 v201, 0xffff0000, v180
	v_lshlrev_b32_e32 v202, 16, v181
	v_and_b32_e32 v203, 0xffff0000, v181
	v_add_f32_e32 v184, v184, v185
	v_add_f32_e32 v1, v1, v184
	v_pk_add_f32 v[184:185], v[136:137], v[200:201]
	v_pk_add_f32 v[194:195], v[138:139], v[202:203]
	v_pk_add_f32 v[184:185], v[184:185], v[190:191]
	v_pk_add_f32 v[186:187], v[194:195], v[186:187]
	v_mul_f32_e32 v190, v185, v185
	v_mul_f32_e32 v191, v187, v187
	v_fmac_f32_e32 v190, v184, v184
	v_fmac_f32_e32 v191, v186, v186
	v_lshlrev_b32_e32 v204, 16, v182
	v_and_b32_e32 v205, 0xffff0000, v182
	v_lshlrev_b32_e32 v206, 16, v183
	v_and_b32_e32 v207, 0xffff0000, v183
	v_add_f32_e32 v190, v190, v191
	v_add_f32_e32 v1, v1, v190
	v_pk_add_f32 v[194:195], v[116:117], v[204:205]
	v_pk_add_f32 v[190:191], v[118:119], v[206:207]
	v_lshl_add_u64 v[2:3], s[38:39], 2, v[232:233]
	v_pk_add_f32 v[190:191], v[190:191], v[188:189]
	v_pk_add_f32 v[188:189], v[194:195], v[192:193]
	v_mul_f32_e32 v193, v191, v191
	v_mul_f32_e32 v192, v189, v189
	v_fmac_f32_e32 v192, v188, v188
	v_fmac_f32_e32 v193, v190, v190
	v_add_f32_e32 v192, v192, v193
	v_add_f32_e32 v1, v1, v192
	s_nop 1
	v_add_f32_dpp v1, v1, v1 quad_perm:[1,0,3,2] row_mask:0xf bank_mask:0xf bound_ctrl:1
	s_nop 1
	v_add_f32_dpp v1, v1, v1 quad_perm:[2,3,0,1] row_mask:0xf bank_mask:0xf bound_ctrl:1
	s_nop 1
	v_add_f32_dpp v1, v1, v1 row_half_mirror row_mask:0xf bank_mask:0xf bound_ctrl:1
	s_nop 1
	v_add_f32_dpp v1, v1, v1 row_mirror row_mask:0xf bank_mask:0xf bound_ctrl:1
	v_mov_b32_e32 v192, v1
	s_nop 1
	v_permlane16_swap_b32_e32 v1, v192
	v_add_f32_e32 v1, v1, v192
	v_mov_b32_e32 v192, v1
	s_nop 1
	v_permlane32_swap_b32_e32 v1, v192
	v_add_f32_e32 v1, v1, v192
	v_fmamk_f32 v1, v1, 0x3a800000, v244
	v_cmp_gt_f32_e32 vcc, s69, v1
	v_mul_f32_e32 v192, 0x4f800000, v1
	s_nop 0
	v_cndmask_b32_e32 v1, v1, v192, vcc
	v_sqrt_f32_e32 v192, v1
	s_nop 0
	v_add_u32_e32 v193, -1, v192
	v_fma_f32 v194, -v193, v192, v1
	v_cmp_ge_f32_e64 s[38:39], 0, v194
	v_add_u32_e32 v194, 1, v192
	s_nop 0
	v_cndmask_b32_e64 v193, v192, v193, s[38:39]
	v_fma_f32 v192, -v194, v192, v1
	v_cmp_lt_f32_e64 s[38:39], 0, v192
	s_nop 1
	v_cndmask_b32_e64 v192, v193, v194, s[38:39]
	v_mul_f32_e32 v193, 0x37800000, v192
	v_cndmask_b32_e32 v192, v192, v193, vcc
	v_cmp_class_f32_e32 vcc, v1, v242
	s_nop 1
	v_cndmask_b32_e32 v1, v192, v1, vcc
	v_div_scale_f32 v192, s[38:39], v1, v1, 1.0
	v_rcp_f32_e32 v193, v192
	s_mov_b64 s[38:39], -1
	v_fma_f32 v194, -v192, v193, 1.0
	v_fmac_f32_e32 v193, v194, v193
	v_div_scale_f32 v194, vcc, 1.0, v1, 1.0
	v_mul_f32_e32 v195, v194, v193
	v_fma_f32 v196, -v192, v195, v194
	v_fmac_f32_e32 v195, v196, v193
	v_fma_f32 v192, -v192, v195, v194
	v_div_fmas_f32 v192, v192, v193, v195
	v_div_fixup_f32 v236, v192, v1, 1.0
	ds_read_b128 v[192:195], v246 offset:48
	ds_read_b128 v[196:199], v246 offset:32
	ds_read_b128 v[200:203], v246 offset:16
	ds_read_b128 v[204:207], v246
	v_pk_mul_f32 v[238:239], v[168:169], v[236:237] op_sel_hi:[1,0]
	v_pk_mul_f32 v[240:241], v[170:171], v[236:237] op_sel_hi:[1,0]
	s_andn2_b64 vcc, exec, s[36:37]
	s_waitcnt lgkmcnt(0)
	v_pk_mul_f32 v[204:205], v[204:205], v[238:239]
	v_pk_mul_f32 v[238:239], v[172:173], v[236:237] op_sel_hi:[1,0]
	v_pk_mul_f32 v[206:207], v[206:207], v[240:241]
	v_pk_mul_f32 v[240:241], v[174:175], v[236:237] op_sel_hi:[1,0]
	v_pk_mul_f32 v[200:201], v[200:201], v[238:239]
	v_pk_mul_f32 v[238:239], v[184:185], v[236:237] op_sel_hi:[1,0]
	v_pk_mul_f32 v[202:203], v[202:203], v[240:241]
	v_pk_mul_f32 v[240:241], v[186:187], v[236:237] op_sel_hi:[1,0]
	v_pk_mul_f32 v[196:197], v[196:197], v[238:239]
	v_pk_mul_f32 v[238:239], v[188:189], v[236:237] op_sel_hi:[1,0]
	v_pk_mul_f32 v[236:237], v[190:191], v[236:237] op_sel_hi:[1,0]
	v_pk_mul_f32 v[198:199], v[198:199], v[240:241]
	v_pk_mul_f32 v[194:195], v[194:195], v[236:237]
	v_pk_mul_f32 v[192:193], v[192:193], v[238:239]
	s_cbranch_vccnz .LBB0_1814
	s_lshr_b64 s[38:39], s[52:53], 12
	s_add_u32 s38, s38, s52
	s_addc_u32 s39, s39, s53
	s_lshl_b64 s[38:39], s[38:39], 11
	s_add_u32 s38, s18, s38
	s_addc_u32 s39, s19, s39
	global_store_dwordx4 v[2:3], v[168:171], off
	global_store_dwordx4 v[2:3], v[172:175], off offset:16
	global_store_dwordx4 v[2:3], v[184:187], off offset:32
	global_store_dwordx4 v[2:3], v[188:191], off offset:48
	v_cvt_pk_bf16_f32 v168, v204, v205
	v_cvt_pk_bf16_f32 v169, v206, v207
	v_cvt_pk_bf16_f32 v170, v200, v201
	v_cvt_pk_bf16_f32 v171, v202, v203
	s_nop 0
	v_lshl_add_u64 v[184:185], v[224:225], 1, s[38:39]
	v_lshl_add_u64 v[186:187], v[184:185], 0, s[16:17]
	v_add_co_u32_e32 v184, vcc, 0x12400000, v184
	s_mov_b64 s[38:39], 0
	s_nop 0
	v_addc_co_u32_e32 v185, vcc, 0, v185, vcc
	v_cvt_pk_bf16_f32 v172, v196, v197
	v_cvt_pk_bf16_f32 v173, v198, v199
	v_cvt_pk_bf16_f32 v174, v192, v193
	v_cvt_pk_bf16_f32 v175, v194, v195
	global_store_dwordx4 v[184:185], v[168:171], off offset:2048
	global_store_dwordx4 v[186:187], v[172:175], off offset:16

.LBB0_1820:
	s_mov_b32 s58, s57
.LBB0_1821:
	s_and_b32 s30, s38, 0xff
	s_add_i32 s30, s30, 15
	s_and_b32 s30, s30, 0x1f0
	s_min_u32 s48, s30, 0x80
	s_bfe_u32 s30, s38, 0x80008
	s_add_i32 s30, s30, 15
	s_and_b32 s30, s30, 0x1f0
	s_min_u32 s60, s30, 0x80
	s_bfe_u32 s30, s38, 0x80010
	s_add_i32 s30, s30, 15
	s_and_b32 s30, s30, 0x1f0
	s_min_u32 s61, s30, 0x80
	s_and_b64 s[38:39], s[6:7], exec
	s_cselect_b32 s30, s60, s61
	s_and_b64 s[38:39], s[40:41], exec
	s_cselect_b32 s30, s48, s30
	s_and_b64 s[38:39], s[42:43], exec
	s_cselect_b32 s30, 0, s30
	s_lshr_b32 s38, s30, 4
	s_min_u32 s70, s38, 7
	s_cmp_lg_u32 s59, s70
	s_cbranch_scc1 .LBB0_1832
	s_ashr_i32 s38, s57, 31
	s_add_u32 s52, s0, s57
	s_addc_u32 s53, s1, s38
	s_lshl_b64 s[38:39], s[52:53], 12
	v_cndmask_b32_e64 v1, 0, 1, s[44:45]
	v_lshl_add_u64 v[2:3], v[232:233], 0, s[38:39]
	v_cmp_ne_u32_e64 s[38:39], 1, v1
	s_andn2_b64 vcc, exec, s[44:45]
	s_cbranch_vccnz .LBB0_1833
	global_load_dwordx4 v[128:131], v[2:3], off
	s_and_b64 vcc, exec, s[38:39]
	s_cbranch_vccz .LBB0_1834

; #define PL_LOAD(RB, TAB, SE, BB) do { _Pragma("unroll") for (int _q = 0; _q < 16; ++_q) { \
;         const unsigned _pw = (unsigned)__builtin_amdgcn_readlane((int)(SE), (BB) * 8 + (_q >> 1)); const unsigned _idx = (_q & 1) ? (_pw >> 16) : (_pw & 0xffffu); \
;         (RB)[_q] = *(const v4u*)((TAB) + (size_t)_idx * 1024 + 16 * lane); } } while (0)
; #define V_ADV() do { ++lb; if (lb >= lbh) { ++lt; if (lt < 16) { V_RANGE(lt, ps, _r0, _r1, _b0, _b1); lb = _b0; lbh = _b1; (void)_r0; (void)_r1; seL = sIdx[lt * 64 + lane]; } } } while (0)
; #define V_SETC() do { ct = lt; cb = lb; { V_RANGE(ct, ps, _r0, _r1, _b0, _b1); crl = _r0; crh = _r1; cbl = _b0; cbh = _b1; } } while (0)
; __device__ __forceinline__ void peer_unit(Frame& F, const Args& a, int layer, int unit, bool last) {
;     ...
;             if (lt < 16) PL_LOAD(rb, V8, seL, lb);
;             V_COMPUTE(ra);
;             if (lt >= 16) break;
;             V_SETC(); V_ADV();
;             if (lt < 16) PL_LOAD(ra, V8, seL, lb);
.LBB0_1842:
	s_and_b64 s[38:39], s[6:7], exec
	s_cselect_b32 s52, s61, 0x80
	s_and_b64 s[38:39], s[40:41], exec
	s_cselect_b32 s52, s60, s52
	s_and_b64 s[38:39], s[42:43], exec
	s_cselect_b32 s39, s48, s52
	s_lshl_b32 s52, s57, 9
	s_add_i32 s52, s15, s52
	s_lshl_b32 s53, s59, 6
	s_add_i32 s52, s52, s53
	v_mov_b32_e32 v176, s52
	s_lshr_b32 s38, s39, 4
	s_add_i32 s70, s70, 1
	ds_read_b128 v[178:181], v176
	s_cmp_gt_i32 s58, 15
	s_cbranch_scc1 .Lpv_skip2
	s_mov_b32 s101, 0
	s_lshl_b32 vcc_lo, s56, 3
	s_waitcnt lgkmcnt(0)
	v_readlane_b32 vcc_hi, v250, vcc_lo
	s_lshl_b32 s100, vcc_hi, 10
	s_and_b32 s100, s100, 0x3fffc00
	v_lshl_add_u64 v[2:3], v[226:227], 0, s[100:101]
	s_bfe_u32 s100, vcc_hi, 0x100010
	s_lshl_b32 s100, s100, 10
	v_lshl_add_u64 v[72:73], v[226:227], 0, s[100:101]
	s_or_b32 s100, vcc_lo, 1
	v_readlane_b32 vcc_hi, v250, s100
	s_lshl_b32 s100, vcc_hi, 10
	s_and_b32 s100, s100, 0x3fffc00
	global_load_dwordx4 v[68:71], v[2:3], off
	s_nop 0
	global_load_dwordx4 v[72:75], v[72:73], off
	v_lshl_add_u64 v[2:3], v[226:227], 0, s[100:101]
	s_bfe_u32 s100, vcc_hi, 0x100010
	s_lshl_b32 s100, s100, 10
	v_lshl_add_u64 v[80:81], v[226:227], 0, s[100:101]
	s_or_b32 s100, vcc_lo, 2
	v_readlane_b32 vcc_hi, v250, s100
	s_lshl_b32 s100, vcc_hi, 10
	s_and_b32 s100, s100, 0x3fffc00
	global_load_dwordx4 v[76:79], v[2:3], off
	s_nop 0
	global_load_dwordx4 v[80:83], v[80:81], off
	v_lshl_add_u64 v[2:3], v[226:227], 0, s[100:101]
	s_bfe_u32 s100, vcc_hi, 0x100010
	s_lshl_b32 s100, s100, 10
	v_lshl_add_u64 v[88:89], v[226:227], 0, s[100:101]
	s_or_b32 s100, vcc_lo, 3
	v_readlane_b32 vcc_hi, v250, s100
	s_lshl_b32 s100, vcc_hi, 10
	s_and_b32 s100, s100, 0x3fffc00
	global_load_dwordx4 v[84:87], v[2:3], off
	s_nop 0
	global_load_dwordx4 v[88:91], v[88:89], off
	v_lshl_add_u64 v[2:3], v[226:227], 0, s[100:101]
	s_bfe_u32 s100, vcc_hi, 0x100010
	s_lshl_b32 s100, s100, 10
	v_lshl_add_u64 v[96:97], v[226:227], 0, s[100:101]
	s_or_b32 s100, vcc_lo, 4
	v_readlane_b32 vcc_hi, v250, s100
	s_lshl_b32 s100, vcc_hi, 10
	s_and_b32 s100, s100, 0x3fffc00
	global_load_dwordx4 v[92:95], v[2:3], off
	s_nop 0
	global_load_dwordx4 v[96:99], v[96:97], off
	v_lshl_add_u64 v[2:3], v[226:227], 0, s[100:101]
	s_bfe_u32 s100, vcc_hi, 0x100010
	s_lshl_b32 s100, s100, 10
	v_lshl_add_u64 v[104:105], v[226:227], 0, s[100:101]
	s_or_b32 s100, vcc_lo, 5
	v_readlane_b32 vcc_hi, v250, s100
	s_lshl_b32 s100, vcc_hi, 10
	s_and_b32 s100, s100, 0x3fffc00
	global_load_dwordx4 v[100:103], v[2:3], off
	s_nop 0
	global_load_dwordx4 v[104:107], v[104:105], off
	v_lshl_add_u64 v[2:3], v[226:227], 0, s[100:101]
	s_bfe_u32 s100, vcc_hi, 0x100010
	s_lshl_b32 s100, s100, 10
	v_lshl_add_u64 v[112:113], v[226:227], 0, s[100:101]
	s_or_b32 s100, vcc_lo, 6
	v_readlane_b32 vcc_hi, v250, s100
	s_lshl_b32 s100, vcc_hi, 10
	s_and_b32 s100, s100, 0x3fffc00
	global_load_dwordx4 v[108:111], v[2:3], off
	s_nop 0
	global_load_dwordx4 v[112:115], v[112:113], off
	v_lshl_add_u64 v[2:3], v[226:227], 0, s[100:101]
	s_bfe_u32 s100, vcc_hi, 0x100010
	s_lshl_b32 s100, s100, 10
	v_lshl_add_u64 v[124:125], v[226:227], 0, s[100:101]
	s_or_b32 s100, vcc_lo, 7
	v_readlane_b32 vcc_lo, v250, s100
	s_lshl_b32 s100, vcc_lo, 10
	s_and_b32 s100, s100, 0x3fffc00
	global_load_dwordx4 v[120:123], v[2:3], off
	s_nop 0
	global_load_dwordx4 v[124:127], v[124:125], off
	v_lshl_add_u64 v[2:3], v[226:227], 0, s[100:101]
	s_bfe_u32 s100, vcc_lo, 0x100010
	s_lshl_b32 s100, s100, 10
	v_lshl_add_u64 v[148:149], v[226:227], 0, s[100:101]
	global_load_dwordx4 v[144:147], v[2:3], off
	s_nop 0
	global_load_dwordx4 v[148:151], v[148:149], off
	s_waitcnt vmcnt(16)
	s_branch .Lpv_go2

.Lpv_go2:
	s_max_u32 s38, s38, s70
	s_lshl_b32 s48, s59, 4
	s_cmp_ge_i32 s48, s30
	s_cselect_b64 s[52:53], -1, 0
	s_cmp_lt_i32 s48, s39
	s_cselect_b64 s[54:55], -1, 0
	s_waitcnt lgkmcnt(0)
	v_mul_f32_e32 v1, 0x45000000, v178
	s_and_b64 vcc, s[52:53], s[54:55]
	v_cndmask_b32_e32 v1, 0, v1, vcc
	v_mov_b32_e32 v2, v0
	s_or_b32 s54, s48, 1
	v_cvt_pk_fp8_f32 v2, v1, v1
	s_cmp_ge_i32 s54, s30
	s_cselect_b64 s[52:53], -1, 0
	s_cmp_lt_i32 s54, s39
	s_cselect_b64 s[54:55], -1, 0
	v_mul_f32_e32 v177, 0x45000000, v179
	s_and_b64 vcc, s[52:53], s[54:55]
	v_cvt_pk_fp8_f32 v2, v1, v1 op_sel:[0,0,1]
	v_cndmask_b32_e32 v177, 0, v177, vcc
	v_mov_b32_e32 v178, v0
	v_cvt_pk_fp8_f32 v178, v177, v177
	v_and_b32_e32 v2, v2, v249
	v_mov_b32_e32 v3, v0
	s_or_b32 s54, s48, 2
	v_cvt_pk_fp8_f32 v178, v177, v177 op_sel:[0,0,1]
	s_cmp_ge_i32 s54, s30
	s_cselect_b64 s[52:53], -1, 0
	s_cmp_lt_i32 s54, s39
	s_cselect_b64 s[54:55], -1, 0
	v_mul_f32_e32 v177, 0x45000000, v180
	s_and_b64 vcc, s[52:53], s[54:55]
	v_mfma_f32_16x16x32_fp8_fp8 v[160:163], v[2:3], v[4:5], v[160:163]
	v_mov_b32_e32 v1, v2
	v_cndmask_b32_e32 v177, 0, v177, vcc
	s_or_b32 s54, s48, 3
	v_mfma_f32_16x16x32_fp8_fp8 v[152:155], v[2:3], v[6:7], v[152:155]
	v_and_b32_e32 v2, v178, v249
	v_mov_b32_e32 v178, v0
	v_cvt_pk_fp8_f32 v178, v177, v177
	v_mfma_f32_16x16x32_fp8_fp8 v[164:167], v[0:1], v[4:5], v[164:167]
	s_cmp_ge_i32 s54, s30
	s_cselect_b64 s[52:53], -1, 0
	v_cvt_pk_fp8_f32 v178, v177, v177 op_sel:[0,0,1]
	v_mfma_f32_16x16x32_fp8_fp8 v[156:159], v[0:1], v[6:7], v[156:159]
	v_mov_b32_e32 v1, v2
	s_cmp_lt_i32 s54, s39
	s_cselect_b64 s[54:55], -1, 0
	v_mfma_f32_16x16x32_fp8_fp8 v[160:163], v[2:3], v[8:9], v[160:163]
	s_and_b64 vcc, s[52:53], s[54:55]
	s_or_b32 s54, s48, 4
	s_cmp_ge_i32 s54, s30
	v_mfma_f32_16x16x32_fp8_fp8 v[152:155], v[2:3], v[10:11], v[152:155]
	v_and_b32_e32 v2, v178, v249
	v_mov_b32_e32 v178, v0
	s_cselect_b64 s[52:53], -1, 0
	v_mfma_f32_16x16x32_fp8_fp8 v[182:185], v[2:3], v[12:13], v[160:163]
	s_cmp_lt_i32 s54, s39
	s_nop 1
	v_mul_f32_e32 v160, 0x45000000, v181
	v_cndmask_b32_e32 v177, 0, v160, vcc
	v_cvt_pk_fp8_f32 v178, v177, v177
	v_mfma_f32_16x16x32_fp8_fp8 v[164:167], v[0:1], v[8:9], v[164:167]
	s_cselect_b64 s[54:55], -1, 0
	s_and_b64 vcc, s[52:53], s[54:55]
	v_cvt_pk_fp8_f32 v178, v177, v177 op_sel:[0,0,1]
	v_mfma_f32_16x16x32_fp8_fp8 v[156:159], v[0:1], v[10:11], v[156:159]
	v_mov_b32_e32 v1, v2
	s_or_b32 s54, s48, 5
	s_cmp_ge_i32 s54, s30
	v_mfma_f32_16x16x32_fp8_fp8 v[160:163], v[2:3], v[14:15], v[152:155]
	v_and_b32_e32 v2, v178, v249
	ds_read_b128 v[178:181], v176 offset:16
	s_cselect_b64 s[52:53], -1, 0
	s_cmp_lt_i32 s54, s39
	s_cselect_b64 s[54:55], -1, 0
	v_mfma_f32_16x16x32_fp8_fp8 v[164:167], v[0:1], v[12:13], v[164:167]
	s_waitcnt lgkmcnt(0)
	v_mul_f32_e32 v177, 0x45000000, v178
	v_cndmask_b32_e32 v177, 0, v177, vcc
	v_mov_b32_e32 v178, v0
	v_cvt_pk_fp8_f32 v178, v177, v177
	s_and_b64 vcc, s[52:53], s[54:55]
	v_mfma_f32_16x16x32_fp8_fp8 v[156:159], v[0:1], v[14:15], v[156:159]
	v_mov_b32_e32 v1, v2
	v_cvt_pk_fp8_f32 v178, v177, v177 op_sel:[0,0,1]
	v_mul_f32_e32 v177, 0x45000000, v179
	v_mfma_f32_16x16x32_fp8_fp8 v[152:155], v[2:3], v[16:17], v[182:185]
	v_cndmask_b32_e32 v177, 0, v177, vcc
	s_or_b32 s54, s48, 6
	s_cmp_ge_i32 s54, s30
	v_mfma_f32_16x16x32_fp8_fp8 v[160:163], v[2:3], v[18:19], v[160:163]
	v_and_b32_e32 v2, v178, v249
	v_mov_b32_e32 v178, v0
	v_cvt_pk_fp8_f32 v178, v177, v177
	s_cselect_b64 s[52:53], -1, 0
	s_cmp_lt_i32 s54, s39
	s_cselect_b64 s[54:55], -1, 0
	v_cvt_pk_fp8_f32 v178, v177, v177 op_sel:[0,0,1]
	v_mul_f32_e32 v177, 0x45000000, v180
	s_and_b64 vcc, s[52:53], s[54:55]
	v_mfma_f32_16x16x32_fp8_fp8 v[164:167], v[0:1], v[16:17], v[164:167]
	v_cndmask_b32_e32 v177, 0, v177, vcc
	s_or_b32 s54, s48, 7
	s_cmp_ge_i32 s54, s30
	v_mfma_f32_16x16x32_fp8_fp8 v[156:159], v[0:1], v[18:19], v[156:159]
	v_mov_b32_e32 v1, v2
	s_cselect_b64 s[52:53], -1, 0
	s_cmp_lt_i32 s54, s39
	v_mfma_f32_16x16x32_fp8_fp8 v[152:155], v[2:3], v[20:21], v[152:155]
	s_cselect_b64 s[54:55], -1, 0
	s_and_b64 vcc, s[52:53], s[54:55]
	s_or_b32 s54, s48, 8
	v_mfma_f32_16x16x32_fp8_fp8 v[160:163], v[2:3], v[22:23], v[160:163]
	v_and_b32_e32 v2, v178, v249
	v_mov_b32_e32 v178, v0
	v_cvt_pk_fp8_f32 v178, v177, v177
	v_mfma_f32_16x16x32_fp8_fp8 v[164:167], v[0:1], v[20:21], v[164:167]
	s_cmp_ge_i32 s54, s30
	s_cselect_b64 s[52:53], -1, 0
	v_cvt_pk_fp8_f32 v178, v177, v177 op_sel:[0,0,1]
	v_mul_f32_e32 v177, 0x45000000, v181
	v_mfma_f32_16x16x32_fp8_fp8 v[156:159], v[0:1], v[22:23], v[156:159]
	v_mov_b32_e32 v1, v2
	v_cndmask_b32_e32 v177, 0, v177, vcc
	s_cmp_lt_i32 s54, s39
	v_mfma_f32_16x16x32_fp8_fp8 v[152:155], v[2:3], v[24:25], v[152:155]
	s_cselect_b64 s[54:55], -1, 0
	s_and_b64 vcc, s[52:53], s[54:55]
	s_or_b32 s54, s48, 9
	v_mfma_f32_16x16x32_fp8_fp8 v[160:163], v[2:3], v[26:27], v[160:163]
	v_and_b32_e32 v2, v178, v249
	v_mov_b32_e32 v178, v0
	v_cvt_pk_fp8_f32 v178, v177, v177
	v_mfma_f32_16x16x32_fp8_fp8 v[164:167], v[0:1], v[24:25], v[164:167]
	s_cmp_ge_i32 s54, s30
	s_cselect_b64 s[52:53], -1, 0
	v_cvt_pk_fp8_f32 v178, v177, v177 op_sel:[0,0,1]
	v_mfma_f32_16x16x32_fp8_fp8 v[156:159], v[0:1], v[26:27], v[156:159]
	v_mov_b32_e32 v1, v2
	s_cmp_lt_i32 s54, s39
	s_cselect_b64 s[54:55], -1, 0
	v_mfma_f32_16x16x32_fp8_fp8 v[152:155], v[2:3], v[28:29], v[152:155]
	v_mfma_f32_16x16x32_fp8_fp8 v[160:163], v[2:3], v[30:31], v[160:163]
	v_and_b32_e32 v2, v178, v249
	ds_read_b128 v[178:181], v176 offset:32
	s_waitcnt lgkmcnt(0)
	v_mul_f32_e32 v177, 0x45000000, v178
	v_cndmask_b32_e32 v177, 0, v177, vcc
	v_mov_b32_e32 v178, v0
	v_cvt_pk_fp8_f32 v178, v177, v177
	s_and_b64 vcc, s[52:53], s[54:55]
	v_mfma_f32_16x16x32_fp8_fp8 v[164:167], v[0:1], v[28:29], v[164:167]
	s_or_b32 s54, s48, 10
	v_cvt_pk_fp8_f32 v178, v177, v177 op_sel:[0,0,1]
	v_mul_f32_e32 v177, 0x45000000, v179
	v_mfma_f32_16x16x32_fp8_fp8 v[156:159], v[0:1], v[30:31], v[156:159]
	v_mov_b32_e32 v1, v2
	v_cndmask_b32_e32 v177, 0, v177, vcc
	s_cmp_ge_i32 s54, s30
	v_mfma_f32_16x16x32_fp8_fp8 v[152:155], v[2:3], v[32:33], v[152:155]
	s_cselect_b64 s[52:53], -1, 0
	s_cmp_lt_i32 s54, s39
	s_cselect_b64 s[54:55], -1, 0
	v_mfma_f32_16x16x32_fp8_fp8 v[160:163], v[2:3], v[34:35], v[160:163]
	v_and_b32_e32 v2, v178, v249
	v_mov_b32_e32 v178, v0
	v_cvt_pk_fp8_f32 v178, v177, v177
	s_and_b64 vcc, s[52:53], s[54:55]
	v_mfma_f32_16x16x32_fp8_fp8 v[164:167], v[0:1], v[32:33], v[164:167]
	s_or_b32 s54, s48, 11
	v_cvt_pk_fp8_f32 v178, v177, v177 op_sel:[0,0,1]
	v_mul_f32_e32 v177, 0x45000000, v180
	v_mfma_f32_16x16x32_fp8_fp8 v[156:159], v[0:1], v[34:35], v[156:159]
	v_mov_b32_e32 v1, v2
	v_cndmask_b32_e32 v177, 0, v177, vcc
	s_cmp_ge_i32 s54, s30
	v_mfma_f32_16x16x32_fp8_fp8 v[152:155], v[2:3], v[36:37], v[152:155]
	s_cselect_b64 s[52:53], -1, 0
	s_cmp_lt_i32 s54, s39
	s_cselect_b64 s[54:55], -1, 0
	v_mfma_f32_16x16x32_fp8_fp8 v[160:163], v[2:3], v[38:39], v[160:163]
	v_and_b32_e32 v2, v178, v249
	v_mov_b32_e32 v178, v0
	v_cvt_pk_fp8_f32 v178, v177, v177
	s_and_b64 vcc, s[52:53], s[54:55]
	v_mfma_f32_16x16x32_fp8_fp8 v[164:167], v[0:1], v[36:37], v[164:167]
	s_or_b32 s54, s48, 12
	v_cvt_pk_fp8_f32 v178, v177, v177 op_sel:[0,0,1]
	v_mul_f32_e32 v177, 0x45000000, v181
	v_mfma_f32_16x16x32_fp8_fp8 v[156:159], v[0:1], v[38:39], v[156:159]
	v_mov_b32_e32 v1, v2
	v_cndmask_b32_e32 v177, 0, v177, vcc
	s_cmp_ge_i32 s54, s30
	v_mfma_f32_16x16x32_fp8_fp8 v[152:155], v[2:3], v[40:41], v[152:155]
	s_cselect_b64 s[52:53], -1, 0
	s_cmp_lt_i32 s54, s39
	s_cselect_b64 s[54:55], -1, 0
	v_mfma_f32_16x16x32_fp8_fp8 v[160:163], v[2:3], v[42:43], v[160:163]
	v_and_b32_e32 v2, v178, v249
	v_mov_b32_e32 v178, v0
	v_cvt_pk_fp8_f32 v178, v177, v177
	v_mfma_f32_16x16x32_fp8_fp8 v[164:167], v[0:1], v[40:41], v[164:167]
	s_and_b64 vcc, s[52:53], s[54:55]
	v_mov_b32_e32 v180, v0
	v_cvt_pk_fp8_f32 v178, v177, v177 op_sel:[0,0,1]
	v_mfma_f32_16x16x32_fp8_fp8 v[156:159], v[0:1], v[42:43], v[156:159]
	v_mov_b32_e32 v1, v2
	s_or_b32 s54, s48, 13
	s_cmp_ge_i32 s54, s30
	v_mfma_f32_16x16x32_fp8_fp8 v[152:155], v[2:3], v[44:45], v[152:155]
	s_cselect_b64 s[52:53], -1, 0
	s_cmp_lt_i32 s54, s39
	s_cselect_b64 s[54:55], -1, 0
	v_mfma_f32_16x16x32_fp8_fp8 v[160:163], v[2:3], v[46:47], v[160:163]
	v_and_b32_e32 v2, v178, v249
	ds_read_b128 v[176:179], v176 offset:48
	v_mov_b32_e32 v181, v0
	v_mfma_f32_16x16x32_fp8_fp8 v[164:167], v[0:1], v[44:45], v[164:167]
	s_waitcnt lgkmcnt(0)
	v_mul_f32_e32 v176, 0x45000000, v176
	v_cndmask_b32_e32 v176, 0, v176, vcc
	v_cvt_pk_fp8_f32 v180, v176, v176
	s_and_b64 vcc, s[52:53], s[54:55]
	v_mfma_f32_16x16x32_fp8_fp8 v[156:159], v[0:1], v[46:47], v[156:159]
	v_mov_b32_e32 v1, v2
	v_cvt_pk_fp8_f32 v180, v176, v176 op_sel:[0,0,1]
	v_mul_f32_e32 v176, 0x45000000, v177
	v_cndmask_b32_e32 v176, 0, v176, vcc
	v_mov_b32_e32 v177, v0
	v_cvt_pk_fp8_f32 v177, v176, v176
	v_mfma_f32_16x16x32_fp8_fp8 v[152:155], v[2:3], v[48:49], v[152:155]
	s_or_b32 s54, s48, 14
	s_cmp_ge_i32 s54, s30
	v_cvt_pk_fp8_f32 v177, v176, v176 op_sel:[0,0,1]
	v_mfma_f32_16x16x32_fp8_fp8 v[160:163], v[2:3], v[50:51], v[160:163]
	v_and_b32_e32 v2, v180, v249
	s_cselect_b64 s[52:53], -1, 0
	s_cmp_lt_i32 s54, s39
	s_cselect_b64 s[54:55], -1, 0
	v_mul_f32_e32 v176, 0x45000000, v178
	s_and_b64 vcc, s[52:53], s[54:55]
	v_mfma_f32_16x16x32_fp8_fp8 v[164:167], v[0:1], v[48:49], v[164:167]
	v_cndmask_b32_e32 v176, 0, v176, vcc
	s_or_b32 s48, s48, 15
	s_cmp_ge_i32 s48, s30
	v_mfma_f32_16x16x32_fp8_fp8 v[156:159], v[0:1], v[50:51], v[156:159]
	v_mov_b32_e32 v1, v2
	s_cselect_b64 s[52:53], -1, 0
	s_cmp_lt_i32 s48, s39
	v_mfma_f32_16x16x32_fp8_fp8 v[152:155], v[2:3], v[52:53], v[152:155]
	s_cselect_b64 s[54:55], -1, 0
	s_and_b64 vcc, s[52:53], s[54:55]
	s_add_i32 s38, s38, -1
	v_mfma_f32_16x16x32_fp8_fp8 v[160:163], v[2:3], v[54:55], v[160:163]
	v_and_b32_e32 v2, v177, v249
	v_mov_b32_e32 v177, v0
	v_cvt_pk_fp8_f32 v177, v176, v176
	v_mfma_f32_16x16x32_fp8_fp8 v[164:167], v[0:1], v[52:53], v[164:167]
	s_cmp_lg_u32 s59, s38
	v_cvt_pk_fp8_f32 v177, v176, v176 op_sel:[0,0,1]
	v_mul_f32_e32 v176, 0x45000000, v179
	v_mfma_f32_16x16x32_fp8_fp8 v[156:159], v[0:1], v[54:55], v[156:159]
	v_mov_b32_e32 v1, v2
	v_cndmask_b32_e32 v180, 0, v176, vcc
	v_cvt_pk_fp8_f32 v181, v180, v180
	v_mfma_f32_16x16x32_fp8_fp8 v[152:155], v[2:3], v[56:57], v[152:155]
	v_cvt_pk_fp8_f32 v181, v180, v180 op_sel:[0,0,1]
	v_mfma_f32_16x16x32_fp8_fp8 v[160:163], v[2:3], v[58:59], v[160:163]
	v_and_b32_e32 v2, v177, v249
	v_mfma_f32_16x16x32_fp8_fp8 v[164:167], v[0:1], v[56:57], v[164:167]
	v_mfma_f32_16x16x32_fp8_fp8 v[156:159], v[0:1], v[58:59], v[156:159]
	v_mov_b32_e32 v1, v2
	v_mfma_f32_16x16x32_fp8_fp8 v[152:155], v[2:3], v[60:61], v[152:155]
	v_mfma_f32_16x16x32_fp8_fp8 v[176:179], v[2:3], v[62:63], v[160:163]
	v_and_b32_e32 v2, v181, v249
	v_mfma_f32_16x16x32_fp8_fp8 v[164:167], v[0:1], v[60:61], v[164:167]
	v_mfma_f32_16x16x32_fp8_fp8 v[156:159], v[0:1], v[62:63], v[156:159]
	v_mov_b32_e32 v1, v2
	v_mfma_f32_16x16x32_fp8_fp8 v[160:163], v[2:3], v[64:65], v[152:155]
	s_nop 0
	v_mfma_f32_16x16x32_fp8_fp8 v[164:167], v[0:1], v[64:65], v[164:167]
	v_mfma_f32_16x16x32_fp8_fp8 v[152:155], v[2:3], v[66:67], v[176:179]
	v_mfma_f32_16x16x32_fp8_fp8 v[156:159], v[0:1], v[66:67], v[156:159]
	s_cbranch_scc1 .LBB0_1850
; __device__ __forceinline__ void peer_token_end(Frame& F, const Args& a, int layer, bool last, bool final_half, size_t tok, int lane, const f32x2 (&out)[8], const f32x4 (&hpre)[4], const v4u (&gpre)[2], const v4u& p8pre) {
;     float* hp = F.h + tok * 1024 + 16 * lane;
;     f32x4 hv[4], ge[4]; float s = 0.f;
;     f32x4 pe[4];
; #pragma unroll
;     for (int i = 0; i < 4; ++i) { const f32x2 lo = __builtin_amdgcn_cvt_pk_f32_fp8((int)p8pre[i], false), hi = __builtin_amdgcn_cvt_pk_f32_fp8((int)p8pre[i], true);
;         pe[i] = (f32x4){lo.x, lo.y, hi.x, hi.y} * (1.f / 256.f) + (f32x4){out[2 * i].x, out[2 * i].y, out[2 * i + 1].x, out[2 * i + 1].y}; }
;     if (!final_half) {
;         v4u w;
; #pragma unroll
;         for (int i = 0; i < 4; ++i) { const f32x4 s8 = pe[i] * 256.f; int t = 0; t = __builtin_amdgcn_cvt_pk_fp8_f32(s8.x, s8.y, t, false); t = __builtin_amdgcn_cvt_pk_fp8_f32(s8.z, s8.w, t, true); w[i] = (unsigned)t; }
;         *(v4u*)((unsigned char*)(F.ws + WS_P8) + tok * 1024 + 16 * lane) = w;
;         return; }
	s_nop 0
	v_cvt_pk_f32_fp8_e32 v[2:3], v140
	v_cvt_pk_f32_fp8_e32 v[178:179], v141
	v_cvt_pk_f32_fp8_sdwa v[180:181], v141 src0_sel:WORD_1
	v_cvt_pk_f32_fp8_sdwa v[188:189], v142 src0_sel:WORD_1
	v_pk_mul_f32 v[2:3], v[2:3], s[12:13] op_sel_hi:[1,0]
	v_cvt_pk_f32_fp8_e32 v[186:187], v142
	v_pk_fma_f32 v[182:183], v[160:161], s[14:15], v[2:3] op_sel_hi:[1,0,1]
	v_pk_mul_f32 v[2:3], v[178:179], s[12:13] op_sel_hi:[1,0]
	v_pk_mul_f32 v[178:179], v[180:181], s[12:13] op_sel_hi:[1,0]
	v_cvt_pk_f32_fp8_sdwa v[176:177], v140 src0_sel:WORD_1
	v_pk_fma_f32 v[180:181], v[166:167], s[14:15], v[178:179] op_sel_hi:[1,0,1]
	v_pk_mul_f32 v[178:179], v[188:189], s[12:13] op_sel_hi:[1,0]
	v_cvt_pk_f32_fp8_e32 v[188:189], v143
	v_cvt_pk_f32_fp8_sdwa v[192:193], v143 src0_sel:WORD_1
	s_ashr_i32 s30, s57, 31
	s_add_u32 s52, s0, s57
	v_pk_fma_f32 v[184:185], v[164:165], s[14:15], v[2:3] op_sel_hi:[1,0,1]
	v_pk_mul_f32 v[2:3], v[186:187], s[12:13] op_sel_hi:[1,0]
	s_addc_u32 s53, s1, s30
	v_pk_mul_f32 v[176:177], v[176:177], s[12:13] op_sel_hi:[1,0]
	v_pk_fma_f32 v[186:187], v[154:155], s[14:15], v[178:179] op_sel_hi:[1,0,1]
	v_pk_fma_f32 v[190:191], v[152:153], s[14:15], v[2:3] op_sel_hi:[1,0,1]
	v_pk_mul_f32 v[2:3], v[188:189], s[12:13] op_sel_hi:[1,0]
	v_pk_mul_f32 v[178:179], v[192:193], s[12:13] op_sel_hi:[1,0]
	s_lshl_b64 s[38:39], s[52:53], 10
	v_pk_fma_f32 v[176:177], v[162:163], s[14:15], v[176:177] op_sel_hi:[1,0,1]
	v_pk_fma_f32 v[188:189], v[158:159], s[14:15], v[178:179] op_sel_hi:[1,0,1]
	v_pk_fma_f32 v[192:193], v[156:157], s[14:15], v[2:3] op_sel_hi:[1,0,1]
	s_andn2_b64 vcc, exec, s[46:47]
	s_mov_b64 s[54:55], -1
	s_cbranch_vccnz .LBB0_1845
	v_pk_mul_f32 v[2:3], v[182:183], s[8:9] op_sel_hi:[1,0]
	v_mov_b32_e32 v194, v0
	v_cvt_pk_fp8_f32 v194, v2, v3
	v_pk_mul_f32 v[2:3], v[184:185], s[8:9] op_sel_hi:[1,0]
	v_mov_b32_e32 v195, v0
	v_cvt_pk_fp8_f32 v195, v2, v3
	v_pk_mul_f32 v[2:3], v[176:177], s[8:9] op_sel_hi:[1,0]
	v_mov_b32_e32 v196, v0
	v_cvt_pk_fp8_f32 v194, v2, v3 op_sel:[0,0,1]
	v_pk_mul_f32 v[2:3], v[180:181], s[8:9] op_sel_hi:[1,0]
	v_mov_b32_e32 v197, v0
	v_cvt_pk_fp8_f32 v195, v2, v3 op_sel:[0,0,1]
	v_pk_mul_f32 v[2:3], v[190:191], s[8:9] op_sel_hi:[1,0]
	s_mov_b64 s[54:55], 0
	v_cvt_pk_fp8_f32 v196, v2, v3
	v_pk_mul_f32 v[2:3], v[192:193], s[8:9] op_sel_hi:[1,0]
	s_nop 0
	v_cvt_pk_fp8_f32 v197, v2, v3
	v_pk_mul_f32 v[2:3], v[186:187], s[8:9] op_sel_hi:[1,0]
	s_nop 0
	v_cvt_pk_fp8_f32 v196, v2, v3 op_sel:[0,0,1]
	v_pk_mul_f32 v[2:3], v[188:189], s[8:9] op_sel_hi:[1,0]
	s_nop 0
	v_cvt_pk_fp8_f32 v197, v2, v3 op_sel:[0,0,1]
	v_lshl_add_u64 v[2:3], v[234:235], 0, s[38:39]
	global_store_dwordx4 v[2:3], v[194:197], off
; __device__ __forceinline__ void unpk8(const u32x4 w, f32x4& a, f32x4& b) { a = (f32x4){bflo(w.x), bfhi(w.x), bflo(w.y), bfhi(w.y)}; b = (f32x4){bflo(w.z), bfhi(w.z), bflo(w.w), bfhi(w.w)}; }
; __device__ __forceinline__ u32x4 pk8(const f32x4 a, const f32x4 b) { u32x4 w; w.x = cvt_pk_bf16(a[0], a[1]); w.y = cvt_pk_bf16(a[2], a[3]); w.z = cvt_pk_bf16(b[0], b[1]); w.w = cvt_pk_bf16(b[2], b[3]); return w; }
; __device__ __forceinline__ void peer_token_end(Frame& F, const Args& a, int layer, bool last, bool final_half, size_t tok, int lane, const f32x2 (&out)[8], const f32x4 (&hpre)[4], const v4u (&gpre)[2], const v4u& p8pre) {
;     ...
;     unpk8(gpre[0], ge[0], ge[1]); unpk8(gpre[1], ge[2], ge[3]);
; #pragma unroll
;     for (int i = 0; i < 4; ++i) { hv[i] = hpre[i] + ge[i] + pe[i];
;         s += (hv[i].x * hv[i].x + hv[i].y * hv[i].y) + (hv[i].z * hv[i].z + hv[i].w * hv[i].w); }
;     const float rstd = 1.f / sqrtf(wave_sum(s) * (1.f / D) + 1e-6f);
;     const float* g = (last ? a.in[4] : a.in[2] + (size_t)(layer + 1) * 1024) + 16 * lane;
;     f32x4 o[4];
; #pragma unroll
;     for (int i = 0; i < 4; ++i) o[i] = hv[i] * rstd * *(const f32x4*)(g + 4 * i);
;     if (last) {
;     ...
;         { const float pv = ((const float*)(F.ws + WS_CTL))[2048 + PROBE_SCAN - 1];
; #pragma unroll
;           for (int i = 0; i < 4; ++i) o[i] = o[i] + pv; }
;     ...
; #pragma unroll
;         for (int i = 0; i < 4; ++i) *(f32x4*)(hp + 4 * i) = o[i];
;     } else {
; #pragma unroll
;         for (int i = 0; i < 4; ++i) *(f32x4*)(hp + 4 * i) = hv[i];
;         bf16* NX = (bf16*)(F.ws + WS_NX) + NXROW(tok) * 1024 + 16 * lane; const v4u w0 = pk8(o[0], o[1]), w1 = pk8(o[2], o[3]);
;         *(v4u*)NX = w0; *(v4u*)(NX + 8) = w1;
;     }
.LBB0_1845:
	s_andn2_b64 vcc, exec, s[54:55]
	s_cbranch_vccnz .LBB0_1850
	v_lshlrev_b32_e32 v178, 16, v168
	v_and_b32_e32 v179, 0xffff0000, v168
	v_lshlrev_b32_e32 v194, 16, v169
	v_and_b32_e32 v195, 0xffff0000, v169
	v_pk_add_f32 v[236:237], v[128:129], v[178:179]
	v_pk_add_f32 v[178:179], v[130:131], v[194:195]
	v_lshlrev_b32_e32 v196, 16, v170
	v_pk_add_f32 v[178:179], v[178:179], v[176:177]
	v_pk_add_f32 v[176:177], v[236:237], v[182:183]
	v_mul_f32_e32 v182, v179, v179
	v_mul_f32_e32 v1, v177, v177
	v_and_b32_e32 v197, 0xffff0000, v170
	v_lshlrev_b32_e32 v198, 16, v171
	v_and_b32_e32 v199, 0xffff0000, v171
	v_fmac_f32_e32 v1, v176, v176
	v_fmac_f32_e32 v182, v178, v178
	v_add_f32_e32 v1, v1, v182
	v_pk_add_f32 v[194:195], v[132:133], v[196:197]
	v_pk_add_f32 v[182:183], v[134:135], v[198:199]
	v_lshlrev_b32_e32 v200, 16, v172
	v_pk_add_f32 v[182:183], v[182:183], v[180:181]
	v_pk_add_f32 v[180:181], v[194:195], v[184:185]
	v_mul_f32_e32 v185, v183, v183
	v_mul_f32_e32 v184, v181, v181
	v_fmac_f32_e32 v184, v180, v180
	v_fmac_f32_e32 v185, v182, v182
	v_and_b32_e32 v201, 0xffff0000, v172
	v_lshlrev_b32_e32 v202, 16, v173
	v_and_b32_e32 v203, 0xffff0000, v173
	v_add_f32_e32 v184, v184, v185
	v_add_f32_e32 v1, v1, v184
	v_pk_add_f32 v[184:185], v[136:137], v[200:201]
	v_pk_add_f32 v[194:195], v[138:139], v[202:203]
	v_pk_add_f32 v[184:185], v[184:185], v[190:191]
	v_pk_add_f32 v[186:187], v[194:195], v[186:187]
	v_mul_f32_e32 v190, v185, v185
	v_mul_f32_e32 v191, v187, v187
	v_fmac_f32_e32 v190, v184, v184
	v_fmac_f32_e32 v191, v186, v186
	v_lshlrev_b32_e32 v204, 16, v174
	v_and_b32_e32 v205, 0xffff0000, v174
	v_lshlrev_b32_e32 v206, 16, v175
	v_and_b32_e32 v207, 0xffff0000, v175
	v_add_f32_e32 v190, v190, v191
	v_add_f32_e32 v1, v1, v190
	v_pk_add_f32 v[194:195], v[116:117], v[204:205]
	v_pk_add_f32 v[190:191], v[118:119], v[206:207]
	v_lshl_add_u64 v[2:3], s[38:39], 2, v[232:233]
	v_pk_add_f32 v[190:191], v[190:191], v[188:189]
	v_pk_add_f32 v[188:189], v[194:195], v[192:193]
	v_mul_f32_e32 v193, v191, v191
	v_mul_f32_e32 v192, v189, v189
	v_fmac_f32_e32 v192, v188, v188
	v_fmac_f32_e32 v193, v190, v190
	v_add_f32_e32 v192, v192, v193
	v_add_f32_e32 v1, v1, v192
	s_nop 1
	v_add_f32_dpp v1, v1, v1 quad_perm:[1,0,3,2] row_mask:0xf bank_mask:0xf bound_ctrl:1
	s_nop 1
	v_add_f32_dpp v1, v1, v1 quad_perm:[2,3,0,1] row_mask:0xf bank_mask:0xf bound_ctrl:1
	s_nop 1
	v_add_f32_dpp v1, v1, v1 row_half_mirror row_mask:0xf bank_mask:0xf bound_ctrl:1
	s_nop 1
	v_add_f32_dpp v1, v1, v1 row_mirror row_mask:0xf bank_mask:0xf bound_ctrl:1
	v_mov_b32_e32 v192, v1
	s_nop 1
	v_permlane16_swap_b32_e32 v1, v192
	v_add_f32_e32 v1, v1, v192
	v_mov_b32_e32 v192, v1
	s_nop 1
	v_permlane32_swap_b32_e32 v1, v192
	v_add_f32_e32 v1, v1, v192
	v_fmamk_f32 v1, v1, 0x3a800000, v244
	v_cmp_gt_f32_e32 vcc, s69, v1
	v_mul_f32_e32 v192, 0x4f800000, v1
	s_nop 0
	v_cndmask_b32_e32 v1, v1, v192, vcc
	v_sqrt_f32_e32 v192, v1
	s_nop 0
	v_add_u32_e32 v193, -1, v192
	v_fma_f32 v194, -v193, v192, v1
	v_cmp_ge_f32_e64 s[38:39], 0, v194
	v_add_u32_e32 v194, 1, v192
	s_nop 0
	v_cndmask_b32_e64 v193, v192, v193, s[38:39]
	v_fma_f32 v192, -v194, v192, v1
	v_cmp_lt_f32_e64 s[38:39], 0, v192
	s_nop 1
	v_cndmask_b32_e64 v192, v193, v194, s[38:39]
	v_mul_f32_e32 v193, 0x37800000, v192
	v_cndmask_b32_e32 v192, v192, v193, vcc
	v_cmp_class_f32_e32 vcc, v1, v242
	s_nop 1
	v_cndmask_b32_e32 v1, v192, v1, vcc
	v_div_scale_f32 v192, s[38:39], v1, v1, 1.0
	v_rcp_f32_e32 v193, v192
	s_mov_b64 s[38:39], -1
	v_fma_f32 v194, -v192, v193, 1.0
	v_fmac_f32_e32 v193, v194, v193
	v_div_scale_f32 v194, vcc, 1.0, v1, 1.0
	v_mul_f32_e32 v195, v194, v193
	v_fma_f32 v196, -v192, v195, v194
	v_fmac_f32_e32 v195, v196, v193
	v_fma_f32 v192, -v192, v195, v194
	v_div_fmas_f32 v192, v192, v193, v195
	v_div_fixup_f32 v236, v192, v1, 1.0
	ds_read_b128 v[192:195], v246 offset:48
	ds_read_b128 v[196:199], v246 offset:32
	ds_read_b128 v[200:203], v246 offset:16
	ds_read_b128 v[204:207], v246
	v_pk_mul_f32 v[238:239], v[176:177], v[236:237] op_sel_hi:[1,0]
	v_pk_mul_f32 v[240:241], v[178:179], v[236:237] op_sel_hi:[1,0]
	s_andn2_b64 vcc, exec, s[36:37]
	s_waitcnt lgkmcnt(0)
	v_pk_mul_f32 v[204:205], v[204:205], v[238:239]
	v_pk_mul_f32 v[238:239], v[180:181], v[236:237] op_sel_hi:[1,0]
	v_pk_mul_f32 v[206:207], v[206:207], v[240:241]
	v_pk_mul_f32 v[240:241], v[182:183], v[236:237] op_sel_hi:[1,0]
	v_pk_mul_f32 v[200:201], v[200:201], v[238:239]
	v_pk_mul_f32 v[238:239], v[184:185], v[236:237] op_sel_hi:[1,0]
	v_pk_mul_f32 v[202:203], v[202:203], v[240:241]
	v_pk_mul_f32 v[240:241], v[186:187], v[236:237] op_sel_hi:[1,0]
	v_pk_mul_f32 v[196:197], v[196:197], v[238:239]
	v_pk_mul_f32 v[238:239], v[188:189], v[236:237] op_sel_hi:[1,0]
	v_pk_mul_f32 v[236:237], v[190:191], v[236:237] op_sel_hi:[1,0]
	v_pk_mul_f32 v[198:199], v[198:199], v[240:241]
	v_pk_mul_f32 v[194:195], v[194:195], v[236:237]
	v_pk_mul_f32 v[192:193], v[192:193], v[238:239]
	s_cbranch_vccnz .LBB0_1848
	s_lshr_b64 s[38:39], s[52:53], 12
	s_add_u32 s38, s38, s52
	s_addc_u32 s39, s39, s53
	s_lshl_b64 s[38:39], s[38:39], 11
	s_add_u32 s38, s18, s38
	s_addc_u32 s39, s19, s39
	global_store_dwordx4 v[2:3], v[176:179], off
	global_store_dwordx4 v[2:3], v[180:183], off offset:16
	global_store_dwordx4 v[2:3], v[184:187], off offset:32
	global_store_dwordx4 v[2:3], v[188:191], off offset:48
	v_cvt_pk_bf16_f32 v176, v204, v205
	v_cvt_pk_bf16_f32 v177, v206, v207
	v_cvt_pk_bf16_f32 v178, v200, v201
	v_cvt_pk_bf16_f32 v179, v202, v203
	s_nop 0
	v_lshl_add_u64 v[184:185], v[224:225], 1, s[38:39]
	v_lshl_add_u64 v[186:187], v[184:185], 0, s[16:17]
	v_add_co_u32_e32 v184, vcc, 0x12400000, v184
	s_mov_b64 s[38:39], 0
	s_nop 0
	v_addc_co_u32_e32 v185, vcc, 0, v185, vcc
	v_cvt_pk_bf16_f32 v180, v196, v197
	v_cvt_pk_bf16_f32 v181, v198, v199
	v_cvt_pk_bf16_f32 v182, v192, v193
	v_cvt_pk_bf16_f32 v183, v194, v195
	global_store_dwordx4 v[184:185], v[176:179], off offset:2048
	global_store_dwordx4 v[186:187], v[180:183], off offset:16

; __global__ void __launch_bounds__(NWAVES * 64, 2) trunk_fwd(Args args) {
	.amdhsa_kernel _Z9trunk_fwd4Args
		.amdhsa_group_segment_fixed_size 0
		.amdhsa_private_segment_fixed_size 0
		.amdhsa_kernarg_size 528
		.amdhsa_user_sgpr_count 2
		.amdhsa_user_sgpr_dispatch_ptr 0
		.amdhsa_user_sgpr_queue_ptr 0
		.amdhsa_user_sgpr_kernarg_segment_ptr 1
		.amdhsa_user_sgpr_dispatch_id 0
		.amdhsa_user_sgpr_kernarg_preload_length 0
		.amdhsa_user_sgpr_kernarg_preload_offset 0
		.amdhsa_user_sgpr_private_segment_size 0
		.amdhsa_uses_dynamic_stack 0
		.amdhsa_enable_private_segment 0
		.amdhsa_system_sgpr_workgroup_id_x 1
		.amdhsa_system_sgpr_workgroup_id_y 0
		.amdhsa_system_sgpr_workgroup_id_z 0
		.amdhsa_system_sgpr_workgroup_info 0
		.amdhsa_system_vgpr_workitem_id 0
		.amdhsa_next_free_vgpr 256
		.amdhsa_next_free_sgpr 102
		.amdhsa_accum_offset 256
		.amdhsa_reserve_vcc 1
		.amdhsa_float_round_mode_32 0
		.amdhsa_float_round_mode_16_64 0
		.amdhsa_float_denorm_mode_32 3
		.amdhsa_float_denorm_mode_16_64 3
		.amdhsa_dx10_clamp 1
		.amdhsa_ieee_mode 1
		.amdhsa_fp16_overflow 0
		.amdhsa_tg_split 0
		.amdhsa_exception_fp_ieee_invalid_op 0
		.amdhsa_exception_fp_denorm_src 0
		.amdhsa_exception_fp_ieee_div_zero 0
		.amdhsa_exception_fp_ieee_overflow 0
		.amdhsa_exception_fp_ieee_underflow 0
		.amdhsa_exception_fp_ieee_inexact 0
		.amdhsa_exception_int_div_zero 0
	.end_amdhsa_kernel

; __global__ void __launch_bounds__(NWAVES * 64, 2) trunk_fwd(Args args) {
amdhsa.kernels:
  - .agpr_count:     0
    .args:
      - .offset:         0
        .size:           272
        .value_kind:     by_value
      - .offset:         272
        .size:           4
        .value_kind:     hidden_block_count_x
      - .offset:         276
        .size:           4
        .value_kind:     hidden_block_count_y
      - .offset:         280
        .size:           4
        .value_kind:     hidden_block_count_z
      - .offset:         284
        .size:           2
        .value_kind:     hidden_group_size_x
      - .offset:         286
        .size:           2
        .value_kind:     hidden_group_size_y
      - .offset:         288
        .size:           2
        .value_kind:     hidden_group_size_z
      - .offset:         290
        .size:           2
        .value_kind:     hidden_remainder_x
      - .offset:         292
        .size:           2
        .value_kind:     hidden_remainder_y
      - .offset:         294
        .size:           2
        .value_kind:     hidden_remainder_z
      - .offset:         312
        .size:           8
        .value_kind:     hidden_global_offset_x
      - .offset:         320
        .size:           8
        .value_kind:     hidden_global_offset_y
      - .offset:         328
        .size:           8
        .value_kind:     hidden_global_offset_z
      - .offset:         336
        .size:           2
        .value_kind:     hidden_grid_dims
      - .offset:         392
        .size:           4
        .value_kind:     hidden_dynamic_lds_size
    .group_segment_fixed_size: 0
    .kernarg_segment_align: 8
    .kernarg_segment_size: 528
    .language:       OpenCL C
    .language_version:
      - 2
      - 0
    .max_flat_workgroup_size: 512
    .name:           _Z9trunk_fwd4Args
    .private_segment_fixed_size: 0
    .sgpr_count:     108
    .sgpr_spill_count: 326
    .symbol:         _Z9trunk_fwd4Args.kd
    .uniform_work_group_size: 1
    .uses_dynamic_stack: false
    .vgpr_count:     256
    .vgpr_spill_count: 0
    .wavefront_size: 64
